# v63 + removed dead zero-init of mLSTM state-increment accumulators + constant grid size instead of kernarg reload in GEMM/attention unit loops
# speedup vs baseline: 1.0060x; 1.0038x over previous
.LBB0_187:
	v_readlane_b32 s14, v254, 0
	v_readlane_b32 s15, v254, 1
	s_movk_i32 s5, 0x100
	s_add_i32 s46, s46, 1
	s_waitcnt lgkmcnt(0)
	s_mul_i32 s5, s46, s5
	s_add_i32 s5, s5, s96
	s_cmpk_lt_i32 s5, 0x318
	s_cselect_b64 s[16:17], -1, 0
	s_cmpk_gt_i32 s5, 0x317
	s_cbranch_scc1 .LBB0_189
	s_mul_hi_i32 s10, s5, 0x2aaaaaab
	s_lshr_b32 s11, s10, 31
	s_add_i32 s10, s10, s11
	s_mul_i32 s11, s10, -6
	s_add_i32 s12, s11, s5

.LBB0_256:
	s_nop 5
	v_add_f32_e32 v32, v32, v128
	v_div_scale_f32 v33, s[8:9], v32, v32, 1.0
	v_rcp_f32_e32 v34, v33
	v_div_scale_f32 v35, vcc, 1.0, v32, 1.0
	v_readlane_b32 s8, v254, 49
	v_fma_f32 v36, -v33, v34, 1.0
	v_fmac_f32_e32 v34, v36, v34
	v_mul_f32_e32 v36, v35, v34
	v_fma_f32 v37, -v33, v36, v35
	v_fmac_f32_e32 v36, v37, v34
	v_fma_f32 v33, -v33, v36, v35
	v_div_fmas_f32 v33, v33, v34, v36
	v_div_fixup_f32 v34, v33, v32, 1.0
	v_mul_f32_e32 v34, 0x42000000, v34
	v_mul_f32_e32 v0, v0, v34
	v_mul_f32_e32 v1, v1, v34
	v_med3_f32 v35, v0, s20, v143
	v_med3_f32 v1, v1, s20, v143
	v_mov_b32_e32 v0, v80
	v_cvt_pk_fp8_f32 v0, v35, v1
	v_mul_f32_e32 v2, v2, v34
	v_mul_f32_e32 v1, v3, v34
	v_med3_f32 v2, v2, s20, v143
	v_med3_f32 v1, v1, s20, v143
	v_cvt_pk_fp8_f32 v0, v2, v1 op_sel:[0,0,1]
	v_mul_f32_e32 v1, v16, v34
	v_mul_f32_e32 v2, v17, v34
	v_med3_f32 v1, v1, s20, v143
	v_med3_f32 v2, v2, s20, v143
	v_mov_b32_e32 v16, v80
	v_cvt_pk_fp8_f32 v16, v1, v2
	v_mul_f32_e32 v3, v18, v34
	v_mul_f32_e32 v1, v19, v34
	v_med3_f32 v2, v3, s20, v143
	v_med3_f32 v1, v1, s20, v143
	v_cvt_pk_fp8_f32 v16, v2, v1 op_sel:[0,0,1]
	v_mul_f32_e32 v1, v4, v34
	v_mul_f32_e32 v2, v5, v34
	v_med3_f32 v4, v1, s20, v143
	v_med3_f32 v2, v2, s20, v143
	v_mov_b32_e32 v1, v80
	v_cvt_pk_fp8_f32 v1, v4, v2
	v_mul_f32_e32 v3, v6, v34
	v_mul_f32_e32 v2, v7, v34
	v_med3_f32 v3, v3, s20, v143
	v_med3_f32 v2, v2, s20, v143
	v_cvt_pk_fp8_f32 v1, v3, v2 op_sel:[0,0,1]
	v_mul_f32_e32 v2, v20, v34
	v_mul_f32_e32 v3, v21, v34
	v_med3_f32 v2, v2, s20, v143
	v_med3_f32 v3, v3, s20, v143
	v_mov_b32_e32 v17, v80
	v_cvt_pk_fp8_f32 v17, v2, v3
	v_mul_f32_e32 v4, v22, v34
	v_mul_f32_e32 v2, v23, v34
	v_med3_f32 v3, v4, s20, v143
	v_med3_f32 v2, v2, s20, v143
	v_cvt_pk_fp8_f32 v17, v3, v2 op_sel:[0,0,1]
	v_mul_f32_e32 v2, v8, v34
	v_mul_f32_e32 v3, v9, v34
	v_med3_f32 v5, v2, s20, v143
	v_med3_f32 v3, v3, s20, v143
	v_mov_b32_e32 v2, v80
	v_cvt_pk_fp8_f32 v2, v5, v3
	v_mul_f32_e32 v4, v10, v34
	v_mul_f32_e32 v3, v11, v34
	v_med3_f32 v4, v4, s20, v143
	v_med3_f32 v3, v3, s20, v143
	v_cvt_pk_fp8_f32 v2, v4, v3 op_sel:[0,0,1]
	v_mul_f32_e32 v3, v24, v34
	v_mul_f32_e32 v4, v25, v34
	v_med3_f32 v3, v3, s20, v143
	v_med3_f32 v4, v4, s20, v143
	v_mov_b32_e32 v18, v80
	v_cvt_pk_fp8_f32 v18, v3, v4
	v_mul_f32_e32 v5, v26, v34
	v_mul_f32_e32 v3, v27, v34
	v_med3_f32 v4, v5, s20, v143
	v_med3_f32 v3, v3, s20, v143
	v_cvt_pk_fp8_f32 v18, v4, v3 op_sel:[0,0,1]
	v_mul_f32_e32 v3, v12, v34
	v_mul_f32_e32 v4, v13, v34
	v_med3_f32 v6, v3, s20, v143
	v_med3_f32 v4, v4, s20, v143
	v_mov_b32_e32 v3, v80
	v_cvt_pk_fp8_f32 v3, v6, v4
	v_mul_f32_e32 v5, v14, v34
	v_mul_f32_e32 v4, v15, v34
	v_med3_f32 v5, v5, s20, v143
	v_med3_f32 v4, v4, s20, v143
	v_cvt_pk_fp8_f32 v3, v5, v4 op_sel:[0,0,1]
	v_mul_f32_e32 v4, v28, v34
	v_mul_f32_e32 v5, v29, v34
	v_med3_f32 v4, v4, s20, v143
	v_med3_f32 v5, v5, s20, v143
	v_mov_b32_e32 v19, v80
	v_cvt_pk_fp8_f32 v19, v4, v5
	v_lshlrev_b64 v[32:33], 10, v[126:127]
	v_readlane_b32 s9, v254, 50
	v_mul_f32_e32 v6, v30, v34
	v_mul_f32_e32 v4, v31, v34
	v_lshl_add_u64 v[32:33], s[8:9], 0, v[32:33]
	v_lshl_add_u64 v[32:33], v[32:33], 0, s[2:3]
	v_med3_f32 v5, v6, s20, v143
	v_med3_f32 v4, v4, s20, v143
	v_permlane32_swap_b32_e32 v0, v1
	v_permlane32_swap_b32_e32 v2, v3
	v_cvt_pk_fp8_f32 v19, v5, v4 op_sel:[0,0,1]
	v_lshl_add_u64 v[4:5], v[32:33], 0, v[116:117]
	v_permlane32_swap_b32_e32 v0, v2
	v_permlane32_swap_b32_e32 v1, v3
	v_readlane_b32 s8, v254, 0
	global_store_dwordx4 v[4:5], v[0:3], off
	v_readlane_b32 s9, v254, 1
	s_movk_i32 s2, 0x100
	s_add_i32 s21, s21, 1
	v_permlane32_swap_b32_e32 v16, v17
	v_permlane32_swap_b32_e32 v18, v19
	s_waitcnt lgkmcnt(0)
	s_mul_i32 s2, s2, s21
	s_add_i32 s12, s2, s96
	v_permlane32_swap_b32_e32 v16, v18
	v_permlane32_swap_b32_e32 v17, v19
	s_cmpk_gt_i32 s12, 0x83f
	global_store_dwordx4 v[4:5], v[16:19], off offset:32
	s_cbranch_scc1 .LBB0_284

.LBB0_347:
	v_readlane_b32 s10, v254, 0
	v_readlane_b32 s11, v254, 1
	s_movk_i32 s7, 0x100
	s_add_i32 s43, s43, 1
	s_waitcnt lgkmcnt(0)
	s_mul_i32 s7, s43, s7
	s_add_i32 s7, s7, s96
	s_cmpk_lt_i32 s7, 0x210
	s_cselect_b64 s[12:13], -1, 0
	s_cmpk_gt_i32 s7, 0x20f
	s_cbranch_scc1 .LBB0_349
	s_ashr_i32 s6, s7, 31
	s_lshr_b32 s6, s6, 30
	s_add_i32 s8, s7, s6
	s_ashr_i32 s6, s8, 2
	s_and_b32 s8, s8, -4
	s_sub_i32 s8, s7, s8

.LBB0_517:
	v_readlane_b32 s2, v254, 0
	v_readlane_b32 s3, v254, 1
	s_movk_i32 s2, 0x100
	s_add_i32 s45, s45, 1
	v_mov_b32_e32 v0, s64
	ds_read_b32 v0, v0
	s_waitcnt lgkmcnt(0)
	s_mul_i32 s2, s45, s2
	s_add_i32 s2, s2, s96
	s_ashr_i32 s3, s2, 31
	s_lshr_b32 s3, s3, 29
	s_add_i32 s3, s2, s3
	s_ashr_i32 s3, s3, 3
	v_readfirstlane_b32 s4, v0
	s_cmp_lt_i32 s3, s4
	s_cselect_b64 s[30:31], -1, 0
	s_cmp_ge_i32 s3, s4
	s_cbranch_scc1 .LBB0_521
	s_lshl_b32 s4, s14, 2
	s_add_i32 s5, s14, -1
	s_add_i32 s4, s4, 0
	s_add_i32 s4, s4, 0x20044
	s_mov_b32 s14, s5

.LBB0_797:
	v_readlane_b32 s10, v254, 0
	v_readlane_b32 s11, v254, 1
	s_movk_i32 s7, 0x100
	s_add_i32 s43, s43, 1
	s_waitcnt lgkmcnt(0)
	s_mul_i32 s7, s43, s7
	s_add_i32 s7, s7, s96
	s_cmpk_lt_i32 s7, 0x630
	s_cselect_b64 s[12:13], -1, 0
	s_cmpk_gt_i32 s7, 0x62f
	s_cbranch_scc1 .LBB0_799
	s_mul_hi_i32 s6, s7, 0x2aaaaaab
	s_lshr_b32 s8, s6, 31
	s_ashr_i32 s6, s6, 1
	s_add_i32 s6, s6, s8
	s_mul_i32 s8, s6, -12
	s_add_i32 s8, s8, s7

.LBB0_880:
	v_max_f32_e32 v2, v4, v4
	v_max_f32_e32 v2, v2, v5
	v_sub_f32_e32 v3, v165, v2
	v_add_f32_e32 v1, v1, v2
	v_mul_f32_e32 v3, 0x3fb8aa3b, v3
	ds_bpermute_b32 v215, v183, v2
	v_add_u32_e32 v2, v184, v186
	v_exp_f32_e32 v3, v3
	s_waitcnt lgkmcnt(0)
	s_barrier
	ds_read_b128 v[152:155], v2
	ds_read_b128 v[144:147], v2 offset:32
	ds_read_b128 v[156:159], v195 offset:17408
	ds_read_b128 v[148:151], v195 offset:17440
	ds_read_b128 v[136:139], v2 offset:64
	ds_read_b128 v[10:13], v2 offset:96
	ds_read_b128 v[140:143], v195 offset:17472
	ds_read_b128 v[132:135], v195 offset:17504
	v_add_u32_e32 v2, v184, v187
	ds_read_b128 v[104:107], v2
	ds_read_b128 v[96:99], v2 offset:32
	v_add_u32_e32 v2, v188, v187
	v_add_u32_e32 v8, s33, v181
	ds_bpermute_b32 v14, v183, v3
	ds_read_b128 v[80:83], v2 offset:55616
	ds_read_b128 v[100:103], v2 offset:55648
	ds_read_b64_tr_b16 v[2:3], v8 offset:51456
	ds_read_b64_tr_b16 v[4:5], v8 offset:51968
	ds_read_b64_tr_b16 v[6:7], v8 offset:52480
	ds_read_b64_tr_b16 v[8:9], v8 offset:52992
	v_xor_b32_e32 v1, 0x80000000, v1
	ds_bpermute_b32 v1, v180, v1
	v_cndmask_b32_e64 v48, 0, 1, s[54:55]
	v_mov_b32_e32 v111, 0
	v_cmp_ne_u32_e64 s[46:47], 1, v48
	s_andn2_b64 vcc, exec, s[54:55]
	s_cbranch_vccnz .LBB0_882
	v_add_u32_e32 v108, s71, v181
	ds_read_b64_tr_b16 v[48:49], v108 offset:34816
	ds_read_b64_tr_b16 v[50:51], v108 offset:35328
	ds_read_b64_tr_b16 v[52:53], v181 offset:51456
	ds_read_b64_tr_b16 v[54:55], v181 offset:51968
	s_mov_b32 s50, s48
	s_mov_b32 s51, s48
	s_mov_b32 s49, s48
	ds_read_b64_tr_b16 v[84:85], v108 offset:35840
	v_mov_b64_e32 v[90:91], s[50:51]
	s_waitcnt lgkmcnt(1)
	v_mfma_f32_32x32x16_bf16 v[64:79], v[48:51], v[52:55], 0
	v_mov_b64_e32 v[88:89], s[48:49]
	ds_read_b64_tr_b16 v[86:87], v108 offset:36352
	ds_read_b64_tr_b16 v[92:93], v181 offset:52480
	ds_read_b64_tr_b16 v[94:95], v181 offset:52992
	v_mfma_f32_32x32x16_bf16 v[48:63], v[48:51], v[88:91], 0
	s_waitcnt lgkmcnt(0)
	v_mfma_f32_32x32x16_bf16 v[64:79], v[84:87], v[92:95], v[64:79]
	v_mfma_f32_32x32x16_bf16 v[48:63], v[84:87], v[88:91], v[48:63]
	ds_read_b64_tr_b16 v[84:85], v108 offset:36864
	ds_read_b64_tr_b16 v[86:87], v108 offset:37376
	ds_read_b64_tr_b16 v[92:93], v181 offset:53504
	ds_read_b64_tr_b16 v[94:95], v181 offset:54016
	s_waitcnt lgkmcnt(0)
	v_mfma_f32_32x32x16_bf16 v[64:79], v[84:87], v[92:95], v[64:79]
	ds_read_b64_tr_b16 v[92:93], v108 offset:37888
	v_mfma_f32_32x32x16_bf16 v[48:63], v[84:87], v[88:91], v[48:63]
	ds_read_b64_tr_b16 v[94:95], v108 offset:38400
	ds_read_b64_tr_b16 v[84:85], v181 offset:54528
	ds_read_b64_tr_b16 v[86:87], v181 offset:55040
	s_waitcnt lgkmcnt(0)
	v_mfma_f32_32x32x16_bf16 v[64:79], v[92:95], v[84:87], v[64:79]
	v_mfma_f32_32x32x16_bf16 v[48:63], v[92:95], v[88:91], v[48:63]

.LBB0_1210:
	v_readlane_b32 s2, v254, 0
	v_readlane_b32 s3, v254, 1
	s_movk_i32 s2, 0x100
	s_add_i32 s47, s47, 1
	v_mov_b32_e32 v0, s66
	ds_read_b32 v0, v0
	s_waitcnt lgkmcnt(0)
	s_mul_i32 s2, s47, s2
	s_add_i32 s2, s2, s96
	s_ashr_i32 s3, s2, 31
	s_lshr_b32 s3, s3, 29
	s_add_i32 s3, s2, s3
	s_ashr_i32 s3, s3, 3
	v_readfirstlane_b32 s4, v0
	s_cmp_lt_i32 s3, s4
	s_cselect_b64 s[30:31], -1, 0
	s_cmp_ge_i32 s3, s4
	s_cbranch_scc1 .LBB0_1214
	s_lshl_b32 s4, s14, 2
	s_add_i32 s5, s14, -1
	s_add_i32 s4, s4, 0
	s_add_i32 s4, s4, 0x20044
	s_mov_b32 s14, s5

.LBB0_1555:
	s_nop 1
	v_add_f32_e32 v32, v34, v32
	v_div_scale_f32 v33, s[0:1], v32, v32, 1.0
	v_rcp_f32_e32 v34, v33
	v_div_scale_f32 v35, vcc, 1.0, v32, 1.0
	v_ashrrev_i32_e32 v161, 31, v160
	v_fma_f32 v36, -v33, v34, 1.0
	v_fmac_f32_e32 v34, v36, v34
	v_mul_f32_e32 v36, v35, v34
	v_fma_f32 v37, -v33, v36, v35
	v_fmac_f32_e32 v36, v37, v34
	v_fma_f32 v33, -v33, v36, v35
	v_div_fmas_f32 v33, v33, v34, v36
	v_div_fixup_f32 v34, v33, v32, 1.0
	v_mul_f32_e32 v34, 0x42000000, v34
	v_mul_f32_e32 v0, v0, v34
	v_mul_f32_e32 v1, v1, v34
	v_med3_f32 v35, v0, s2, v208
	v_med3_f32 v1, v1, s2, v208
	v_mov_b32_e32 v0, 0
	v_cvt_pk_fp8_f32 v0, v35, v1
	v_mul_f32_e32 v2, v2, v34
	v_mul_f32_e32 v1, v3, v34
	v_med3_f32 v2, v2, s2, v208
	v_med3_f32 v1, v1, s2, v208
	v_cvt_pk_fp8_f32 v0, v2, v1 op_sel:[0,0,1]
	v_mul_f32_e32 v1, v16, v34
	v_mul_f32_e32 v2, v17, v34
	v_med3_f32 v1, v1, s2, v208
	v_med3_f32 v2, v2, s2, v208
	v_mov_b32_e32 v16, 0
	v_cvt_pk_fp8_f32 v16, v1, v2
	v_mul_f32_e32 v3, v18, v34
	v_mul_f32_e32 v1, v19, v34
	v_med3_f32 v2, v3, s2, v208
	v_med3_f32 v1, v1, s2, v208
	v_cvt_pk_fp8_f32 v16, v2, v1 op_sel:[0,0,1]
	v_mul_f32_e32 v1, v4, v34
	v_mul_f32_e32 v2, v5, v34
	v_med3_f32 v4, v1, s2, v208
	v_med3_f32 v2, v2, s2, v208
	v_mov_b32_e32 v1, 0
	v_cvt_pk_fp8_f32 v1, v4, v2
	v_mul_f32_e32 v3, v6, v34
	v_mul_f32_e32 v2, v7, v34
	v_med3_f32 v3, v3, s2, v208
	v_med3_f32 v2, v2, s2, v208
	v_cvt_pk_fp8_f32 v1, v3, v2 op_sel:[0,0,1]
	v_mul_f32_e32 v2, v20, v34
	v_mul_f32_e32 v3, v21, v34
	v_med3_f32 v2, v2, s2, v208
	v_med3_f32 v3, v3, s2, v208
	v_mov_b32_e32 v17, 0
	v_cvt_pk_fp8_f32 v17, v2, v3
	v_mul_f32_e32 v4, v22, v34
	v_mul_f32_e32 v2, v23, v34
	v_med3_f32 v3, v4, s2, v208
	v_med3_f32 v2, v2, s2, v208
	v_cvt_pk_fp8_f32 v17, v3, v2 op_sel:[0,0,1]
	v_mul_f32_e32 v2, v8, v34
	v_mul_f32_e32 v3, v9, v34
	v_med3_f32 v5, v2, s2, v208
	v_med3_f32 v3, v3, s2, v208
	v_mov_b32_e32 v2, 0
	v_cvt_pk_fp8_f32 v2, v5, v3
	v_mul_f32_e32 v4, v10, v34
	v_mul_f32_e32 v3, v11, v34
	v_med3_f32 v4, v4, s2, v208
	v_med3_f32 v3, v3, s2, v208
	v_cvt_pk_fp8_f32 v2, v4, v3 op_sel:[0,0,1]
	v_mul_f32_e32 v3, v24, v34
	v_mul_f32_e32 v4, v25, v34
	v_med3_f32 v3, v3, s2, v208
	v_med3_f32 v4, v4, s2, v208
	v_mov_b32_e32 v18, 0
	v_cvt_pk_fp8_f32 v18, v3, v4
	v_mul_f32_e32 v5, v26, v34
	v_mul_f32_e32 v3, v27, v34
	v_med3_f32 v4, v5, s2, v208
	v_med3_f32 v3, v3, s2, v208
	v_cvt_pk_fp8_f32 v18, v4, v3 op_sel:[0,0,1]
	v_mul_f32_e32 v3, v12, v34
	v_mul_f32_e32 v4, v13, v34
	v_med3_f32 v6, v3, s2, v208
	v_med3_f32 v4, v4, s2, v208
	v_mov_b32_e32 v3, 0
	v_cvt_pk_fp8_f32 v3, v6, v4
	v_mul_f32_e32 v5, v14, v34
	v_mul_f32_e32 v4, v15, v34
	v_med3_f32 v5, v5, s2, v208
	v_med3_f32 v4, v4, s2, v208
	v_cvt_pk_fp8_f32 v3, v5, v4 op_sel:[0,0,1]
	v_mul_f32_e32 v4, v28, v34
	v_mul_f32_e32 v5, v29, v34
	v_med3_f32 v4, v4, s2, v208
	v_med3_f32 v5, v5, s2, v208
	v_mov_b32_e32 v19, 0
	v_readlane_b32 s0, v254, 49
	v_cvt_pk_fp8_f32 v19, v4, v5
	v_lshlrev_b64 v[32:33], 10, v[160:161]
	v_readlane_b32 s1, v254, 50
	v_mul_f32_e32 v6, v30, v34
	v_mul_f32_e32 v4, v31, v34
	v_lshl_add_u64 v[32:33], s[0:1], 0, v[32:33]
	v_lshl_add_u64 v[32:33], v[32:33], 0, s[80:81]
	v_med3_f32 v5, v6, s2, v208
	v_med3_f32 v4, v4, s2, v208
	v_permlane32_swap_b32_e32 v0, v1
	v_permlane32_swap_b32_e32 v2, v3
	v_cvt_pk_fp8_f32 v19, v5, v4 op_sel:[0,0,1]
	v_lshl_add_u64 v[4:5], v[32:33], 0, v[154:155]
	v_permlane32_swap_b32_e32 v0, v2
	v_permlane32_swap_b32_e32 v1, v3
	v_readlane_b32 s0, v254, 0
	global_store_dwordx4 v[4:5], v[0:3], off
	v_readlane_b32 s1, v254, 1
	s_movk_i32 s0, 0x100
	s_add_i32 s3, s3, 1
	v_readlane_b32 s1, v255, 32
	v_permlane32_swap_b32_e32 v16, v17
	s_waitcnt lgkmcnt(0)
	s_mul_i32 s0, s0, s3
	v_permlane32_swap_b32_e32 v18, v19
	s_add_i32 s21, s0, s1
	s_nop 0
	v_permlane32_swap_b32_e32 v16, v18
	v_permlane32_swap_b32_e32 v17, v19
	s_cmpk_gt_i32 s21, 0x83f
	global_store_dwordx4 v[4:5], v[16:19], off offset:32
	s_cbranch_scc1 .LBB0_1635

.LBB0_2213:
	s_nop 5
	v_add_f32_e32 v32, v32, v128
	v_div_scale_f32 v33, s[8:9], v32, v32, 1.0
	v_rcp_f32_e32 v34, v33
	v_div_scale_f32 v35, vcc, 1.0, v32, 1.0
	v_readlane_b32 s8, v254, 49
	v_fma_f32 v36, -v33, v34, 1.0
	v_fmac_f32_e32 v34, v36, v34
	v_mul_f32_e32 v36, v35, v34
	v_fma_f32 v37, -v33, v36, v35
	v_fmac_f32_e32 v36, v37, v34
	v_fma_f32 v33, -v33, v36, v35
	v_div_fmas_f32 v33, v33, v34, v36
	v_div_fixup_f32 v34, v33, v32, 1.0
	v_mul_f32_e32 v34, 0x42000000, v34
	v_mul_f32_e32 v0, v0, v34
	v_mul_f32_e32 v1, v1, v34
	v_med3_f32 v35, v0, s20, v143
	v_med3_f32 v1, v1, s20, v143
	v_mov_b32_e32 v0, v80
	v_cvt_pk_fp8_f32 v0, v35, v1
	v_mul_f32_e32 v2, v2, v34
	v_mul_f32_e32 v1, v3, v34
	v_med3_f32 v2, v2, s20, v143
	v_med3_f32 v1, v1, s20, v143
	v_cvt_pk_fp8_f32 v0, v2, v1 op_sel:[0,0,1]
	v_mul_f32_e32 v1, v16, v34
	v_mul_f32_e32 v2, v17, v34
	v_med3_f32 v1, v1, s20, v143
	v_med3_f32 v2, v2, s20, v143
	v_mov_b32_e32 v16, v80
	v_cvt_pk_fp8_f32 v16, v1, v2
	v_mul_f32_e32 v3, v18, v34
	v_mul_f32_e32 v1, v19, v34
	v_med3_f32 v2, v3, s20, v143
	v_med3_f32 v1, v1, s20, v143
	v_cvt_pk_fp8_f32 v16, v2, v1 op_sel:[0,0,1]
	v_mul_f32_e32 v1, v4, v34
	v_mul_f32_e32 v2, v5, v34
	v_med3_f32 v4, v1, s20, v143
	v_med3_f32 v2, v2, s20, v143
	v_mov_b32_e32 v1, v80
	v_cvt_pk_fp8_f32 v1, v4, v2
	v_mul_f32_e32 v3, v6, v34
	v_mul_f32_e32 v2, v7, v34
	v_med3_f32 v3, v3, s20, v143
	v_med3_f32 v2, v2, s20, v143
	v_cvt_pk_fp8_f32 v1, v3, v2 op_sel:[0,0,1]
	v_mul_f32_e32 v2, v20, v34
	v_mul_f32_e32 v3, v21, v34
	v_med3_f32 v2, v2, s20, v143
	v_med3_f32 v3, v3, s20, v143
	v_mov_b32_e32 v17, v80
	v_cvt_pk_fp8_f32 v17, v2, v3
	v_mul_f32_e32 v4, v22, v34
	v_mul_f32_e32 v2, v23, v34
	v_med3_f32 v3, v4, s20, v143
	v_med3_f32 v2, v2, s20, v143
	v_cvt_pk_fp8_f32 v17, v3, v2 op_sel:[0,0,1]
	v_mul_f32_e32 v2, v8, v34
	v_mul_f32_e32 v3, v9, v34
	v_med3_f32 v5, v2, s20, v143
	v_med3_f32 v3, v3, s20, v143
	v_mov_b32_e32 v2, v80
	v_cvt_pk_fp8_f32 v2, v5, v3
	v_mul_f32_e32 v4, v10, v34
	v_mul_f32_e32 v3, v11, v34
	v_med3_f32 v4, v4, s20, v143
	v_med3_f32 v3, v3, s20, v143
	v_cvt_pk_fp8_f32 v2, v4, v3 op_sel:[0,0,1]
	v_mul_f32_e32 v3, v24, v34
	v_mul_f32_e32 v4, v25, v34
	v_med3_f32 v3, v3, s20, v143
	v_med3_f32 v4, v4, s20, v143
	v_mov_b32_e32 v18, v80
	v_cvt_pk_fp8_f32 v18, v3, v4
	v_mul_f32_e32 v5, v26, v34
	v_mul_f32_e32 v3, v27, v34
	v_med3_f32 v4, v5, s20, v143
	v_med3_f32 v3, v3, s20, v143
	v_cvt_pk_fp8_f32 v18, v4, v3 op_sel:[0,0,1]
	v_mul_f32_e32 v3, v12, v34
	v_mul_f32_e32 v4, v13, v34
	v_med3_f32 v6, v3, s20, v143
	v_med3_f32 v4, v4, s20, v143
	v_mov_b32_e32 v3, v80
	v_cvt_pk_fp8_f32 v3, v6, v4
	v_mul_f32_e32 v5, v14, v34
	v_mul_f32_e32 v4, v15, v34
	v_med3_f32 v5, v5, s20, v143
	v_med3_f32 v4, v4, s20, v143
	v_cvt_pk_fp8_f32 v3, v5, v4 op_sel:[0,0,1]
	v_mul_f32_e32 v4, v28, v34
	v_mul_f32_e32 v5, v29, v34
	v_med3_f32 v4, v4, s20, v143
	v_med3_f32 v5, v5, s20, v143
	v_mov_b32_e32 v19, v80
	v_cvt_pk_fp8_f32 v19, v4, v5
	v_lshlrev_b64 v[32:33], 10, v[126:127]
	v_readlane_b32 s9, v254, 50
	v_mul_f32_e32 v6, v30, v34
	v_mul_f32_e32 v4, v31, v34
	v_lshl_add_u64 v[32:33], s[8:9], 0, v[32:33]
	v_lshl_add_u64 v[32:33], v[32:33], 0, s[2:3]
	v_med3_f32 v5, v6, s20, v143
	v_med3_f32 v4, v4, s20, v143
	v_permlane32_swap_b32_e32 v0, v1
	v_permlane32_swap_b32_e32 v2, v3
	v_cvt_pk_fp8_f32 v19, v5, v4 op_sel:[0,0,1]
	v_lshl_add_u64 v[4:5], v[32:33], 0, v[116:117]
	v_permlane32_swap_b32_e32 v0, v2
	v_permlane32_swap_b32_e32 v1, v3
	v_readlane_b32 s8, v254, 0
	global_store_dwordx4 v[4:5], v[0:3], off
	v_readlane_b32 s9, v254, 1
	s_movk_i32 s8, 0x100
	s_add_i32 s22, s22, 1
	v_permlane32_swap_b32_e32 v16, v17
	v_permlane32_swap_b32_e32 v18, v19
	s_waitcnt lgkmcnt(0)
	s_mul_i32 s2, s8, s22
	s_add_i32 s2, s2, s96
	s_add_i32 s21, s21, s8
	v_permlane32_swap_b32_e32 v16, v18
	v_permlane32_swap_b32_e32 v17, v19
	s_cmpk_gt_i32 s2, 0x7ff
	global_store_dwordx4 v[4:5], v[16:19], off offset:32
	s_cbranch_scc1 .LBB0_2237

.LBB0_2300:
	v_readlane_b32 s12, v254, 0
	v_readlane_b32 s13, v254, 1
	s_movk_i32 s9, 0x100
	s_add_i32 s45, s45, 1
	s_waitcnt lgkmcnt(0)
	s_mul_i32 s9, s45, s9
	s_add_i32 s9, s9, s96
	s_cmpk_lt_i32 s9, 0x200
	s_cselect_b64 s[14:15], -1, 0
	s_cmpk_gt_i32 s9, 0x1ff
	s_cbranch_scc1 .LBB0_2302
	s_ashr_i32 s8, s9, 31
	s_lshr_b32 s8, s8, 30
	s_add_i32 s10, s9, s8
	s_ashr_i32 s8, s10, 2
	s_and_b32 s10, s10, -4
	s_sub_i32 s10, s9, s10
